# v28 + MLA steady loops: LDS-DMA issues use SGPR base + one 32-bit lane offset instead of 64-bit per-lane addresses; bases advanced by scalar adds
# speedup vs baseline: 1.0029x; 1.0029x over previous
; template <bool FOX>
; __device__ __forceinline__ void attn_unit(const Args& A, int b, int h, int qb, LAS char* shm, LAS float* dg) {
;     ...
;     const bf16_t* Kg = (FOX ? A.Fk : A.Kmla) + (long)(b * 8 + h) * 128 * (KSLOT / 2) + wid * 512 + lane * 8;
;     const bf16_t* Vg = (FOX ? A.Fv : A.Vmla) + (long)(b * 8 + h) * 128 * 4096 + wid * 512 + lane * 8;
;     const unsigned kdst = lds0 + L_K + wid * 1024, vdst = lds0 + L_V + wid * 1024;
;     const bool k2 = (!FOX) && wid < 4;
.LBB0_825:
	s_add_i32 s27, s26, 3
	s_cmp_lt_u32 s27, s94
	s_cbranch_scc0 .LBB0_828
	s_cmp_lg_u32 s98, 0
	s_cbranch_scc0 .Lmla_ss_no
	s_cmp_lg_u32 s26, s59
	s_cbranch_scc0 .Lmla_ss_no
	s_and_b32 s52, s27, 3
	s_mulk_i32 s52, 0x3000
	s_add_i32 s52, s52, s91
	s_add_i32 s53, s42, 0x6000
	s_and_b32 s53, s53, 0x6000
	s_add_i32 s53, s53, s93
	v_readfirstlane_b32 s46, v234
	v_readfirstlane_b32 s47, v235
	v_readfirstlane_b32 s60, v232
	v_readfirstlane_b32 s61, v233
	s_nop 3
	v_subrev_u32_e32 v240, s46, v234
	s_add_u32 s98, s46, s56
	s_addc_u32 s99, s47, s57
	s_add_u32 s60, s60, s42
	s_addc_u32 s61, s61, s43
	s_nop 4
	s_cmp_lt_i32 s89, 4
	s_cbranch_scc1 .Lmla_ss1_in
	s_branch .Lmla_ss2_top

; #define SFENCE() __builtin_amdgcn_sched_barrier(0)
; template <bool FOX>
; __device__ __forceinline__ void attn_unit(const Args& A, int b, int h, int qb, LAS char* shm, LAS float* dg) {
;     ...
;           const lds_cptr vp = vp0 + ((t - 1) % NS) * VSLOT; float sa = 0.f, sb = 0.f;
; #pragma unroll
;           for (int g = 0; g < 2 * NQ; ++g) {
;               if (!FOX && g == 0) c0 = __builtin_amdgcn_mfma_f32_32x32x16_bf16(kf[0], qr[0], negm, 0, 0, 0);
;               else if (!FOX && g == 1) c1 = __builtin_amdgcn_mfma_f32_32x32x16_bf16(kf[1], qr[0], negm, 0, 0, 0);
;               else if (g & 1) c1 = __builtin_amdgcn_mfma_f32_32x32x16_bf16(kf[g], qr[g >> 1], c1, 0, 0, 0); else c0 = __builtin_amdgcn_mfma_f32_32x32x16_bf16(kf[g], qr[g >> 1], c0, 0, 0, 0);
;               if (g < 8) { const int i = (g >> 1) + 4 * (g & 1); vlo[i] = vtr(vp + (i >> 2) * 4096 + (i & 3) * 1024); vhi[i] = vtr(vp + (i >> 2) * 4096 + (i & 3) * 1024 + 512);
;                   if (g < 4) { sa += pp0[4 * g]; sb += pp0[4 * g + 1]; sa += pp0[4 * g + 2]; sb += pp0[4 * g + 3]; } else { sa += pp1[4 * g - 16]; sb += pp1[4 * g - 15]; sa += pp1[4 * g - 14]; sb += pp1[4 * g - 13]; }
;                   asm volatile("" : "+v"(sa), "+v"(sb)); }
;               { constexpr int G0 = FOX ? 0 : 4; if (g >= G0) { const int q = 2 * (g - G0);
; #pragma unroll
;                   for (int k = 0; k < 2; ++k) { const int w = q + k; const unsigned pkd = w < 8 ? cvt_pk_bf16(pp0[2 * w], pp0[2 * w + 1]) : cvt_pk_bf16(pp1[2 * w - 16], pp1[2 * w - 15]); pw[w >> 2][w & 3] = pkd; } } }
;               SFENCE();
;           }
;           lrun += sa + sb; }
;         MASKONLY(t);
;         float rm; ROWMAX(rm);
;         bool resc = false;
;         if (__any(rm > THR)) { const float dl = fmaxf(rm, 0.f); mhat += dl;
; #pragma unroll
;             for (int r = 0; r < 16; ++r) { c0[r] -= dl; c1[r] -= dl; }
;             if constexpr (!FOX) {
; #pragma unroll
;                 for (int r = 0; r < 16; ++r) negm[r] = -mhat;
;                 asm volatile("" : "+v"(negm)); }
;             const float f = __builtin_amdgcn_exp2f(-dl); lrun *= f; if (hi == 0) wsf[r32] = f; resc = true; }
;         SFENCE();
;         { const lds_cptr kp = kp0 + ((t + 1) % NS) * KSLOT;
; #pragma unroll
;           for (int g = 0; g < 8; ++g) { const int i = (g >> 1) + 4 * (g & 1);
.Lmla_ss1_in:
	s_mov_b32 m0, s52
	s_nop 0
	global_load_lds_dwordx4 v240, s[46:47]
	s_add_i32 m0, s52, 0x2000
	s_nop 0
	global_load_lds_dwordx4 v240, s[98:99]
	s_mov_b32 m0, s53
	s_nop 0
	global_load_lds_dwordx4 v240, s[60:61]
	s_waitcnt lgkmcnt(0)
	s_add_i32 s27, s42, 0x8000
	v_mfma_f32_32x32x16_bf16 v[114:129], v[206:209], v[138:141], v[82:97]
	s_and_b32 s27, s27, 0x6000
	s_add_u32 s42, s42, 0x2000
	s_addc_u32 s43, s43, 0
	v_add_u32_e32 v3, s27, v247
	ds_read_b64_tr_b16 v[206:207], v3 offset:49152
	ds_read_b64_tr_b16 v[208:209], v3 offset:49664
	v_add_f32_e32 v4, 0, v67
	v_add_f32_e32 v5, 0, v66
	v_add_f32_e32 v4, v69, v4
	v_add_f32_e32 v5, v68, v5
	v_mfma_f32_32x32x16_bf16 v[98:113], v[194:197], v[138:141], v[82:97]
	ds_read_b64_tr_b16 v[194:195], v3 offset:53248
	ds_read_b64_tr_b16 v[196:197], v3 offset:53760
	v_add_f32_e32 v4, v71, v4
	v_add_f32_e32 v5, v70, v5
	v_add_f32_e32 v4, v73, v4
	v_add_f32_e32 v5, v72, v5
	v_mfma_f32_32x32x16_bf16 v[114:129], v[202:205], v[142:145], v[114:129]
	ds_read_b64_tr_b16 v[202:203], v3 offset:50176
	ds_read_b64_tr_b16 v[204:205], v3 offset:50688
	v_add_f32_e32 v4, v75, v4
	v_add_f32_e32 v5, v74, v5
	v_add_f32_e32 v4, v77, v4
	v_add_f32_e32 v5, v76, v5
	v_mfma_f32_32x32x16_bf16 v[98:113], v[186:189], v[142:145], v[98:113]
	ds_read_b64_tr_b16 v[214:215], v3 offset:54272
	ds_read_b64_tr_b16 v[216:217], v3 offset:54784
	v_add_f32_e32 v4, v79, v4
	v_add_f32_e32 v5, v78, v5
	v_add_f32_e32 v4, v81, v4
	v_add_f32_e32 v5, v80, v5
	v_mfma_f32_32x32x16_bf16 v[114:129], v[198:201], v[146:149], v[114:129]
	ds_read_b64_tr_b16 v[210:211], v3 offset:51200
	ds_read_b64_tr_b16 v[212:213], v3 offset:51712
	v_add_f32_e32 v4, v51, v4
	v_add_f32_e32 v5, v50, v5
	v_add_f32_e32 v4, v53, v4
	v_add_f32_e32 v5, v52, v5
	v_mfma_f32_32x32x16_bf16 v[98:113], v[182:185], v[146:149], v[98:113]
	ds_read_b64_tr_b16 v[12:13], v3 offset:55296
	ds_read_b64_tr_b16 v[14:15], v3 offset:55808
	v_add_f32_e32 v4, v55, v4
	v_add_f32_e32 v5, v54, v5
	v_add_f32_e32 v4, v57, v4
	v_add_f32_e32 v5, v56, v5
	v_mfma_f32_32x32x16_bf16 v[114:129], v[190:193], v[150:153], v[114:129]
	ds_read_b64_tr_b16 v[8:9], v3 offset:52224
	ds_read_b64_tr_b16 v[10:11], v3 offset:52736
	v_add_f32_e32 v4, v59, v4
	v_add_f32_e32 v16, v61, v4
	v_add_f32_e32 v4, v58, v5
	v_add_f32_e32 v17, v60, v4
	v_mfma_f32_32x32x16_bf16 v[98:113], v[170:173], v[150:153], v[98:113]
	s_add_u32 s46, s46, s62
	s_addc_u32 s47, s47, s63
	s_and_b32 s64, s26, 3
	ds_read_b64_tr_b16 v[4:5], v3 offset:56320
	ds_read_b64_tr_b16 v[6:7], v3 offset:56832
	v_add_f32_e32 v3, v63, v16
	v_add_f32_e32 v16, v62, v17
	v_add_f32_e32 v3, v65, v3
	v_add_f32_e32 v16, v64, v16
	v_mfma_f32_32x32x16_bf16 v[114:129], v[178:181], v[154:157], v[114:129]
	s_mulk_i32 s64, 0x3000
	s_add_u32 s60, s60, 0x2000
	s_addc_u32 s61, s61, 0
	v_cvt_pk_bf16_f32 v178, v50, v51
	v_cvt_pk_bf16_f32 v179, v52, v53
	v_cvt_pk_bf16_f32 v186, v66, v67
	v_cvt_pk_bf16_f32 v187, v68, v69
	v_mfma_f32_32x32x16_bf16 v[98:113], v[166:169], v[154:157], v[98:113]
	s_add_i32 s52, s64, s91
	s_add_i32 s64, s42, 0x6000
	s_add_u32 s98, s98, s62
	s_addc_u32 s99, s99, s63
	v_cvt_pk_bf16_f32 v180, v54, v55
	v_cvt_pk_bf16_f32 v181, v56, v57
	v_cvt_pk_bf16_f32 v188, v70, v71
	v_cvt_pk_bf16_f32 v189, v72, v73
	v_mfma_f32_32x32x16_bf16 v[114:129], v[174:177], v[158:161], v[114:129]
	s_and_b32 s64, s64, 0x6000
	s_add_i32 s53, s64, s93
	v_cvt_pk_bf16_f32 v218, v58, v59
	v_cvt_pk_bf16_f32 v219, v60, v61
	v_cvt_pk_bf16_f32 v182, v74, v75
	v_cvt_pk_bf16_f32 v183, v76, v77
	v_mfma_f32_32x32x16_bf16 v[98:113], v[162:165], v[158:161], v[98:113]
	v_cvt_pk_bf16_f32 v220, v62, v63
	v_cvt_pk_bf16_f32 v221, v64, v65
	v_cvt_pk_bf16_f32 v184, v78, v79
	v_cvt_pk_bf16_f32 v185, v80, v81
	v_add_f32_e32 v3, v3, v16
	v_add_f32_e32 v246, v246, v3
	s_nop 3
	s_waitcnt lgkmcnt(0)
	v_mfma_f32_32x32x16_bf16 v[18:33], v[186:189], v[206:209], v[18:33]
	s_add_i32 s27, s26, 1
	s_and_b32 s64, s27, 3
	s_mulk_i32 s64, 0x3000
	v_exp_f32_e32 v66, v114
	v_exp_f32_e32 v67, v115
	v_exp_f32_e32 v68, v116
	v_exp_f32_e32 v69, v117
	v_add_u32_e32 v3, s64, v248
	v_mfma_f32_32x32x16_bf16 v[34:49], v[186:189], v[194:197], v[34:49]
	v_exp_f32_e32 v70, v118
	v_exp_f32_e32 v71, v119
	v_exp_f32_e32 v72, v120
	v_exp_f32_e32 v73, v121
	ds_read_b128 v[206:209], v3
	ds_read_b128 v[194:197], v3 offset:512
	v_mfma_f32_32x32x16_bf16 v[18:33], v[182:185], v[202:205], v[18:33]
	v_exp_f32_e32 v74, v122
	v_exp_f32_e32 v75, v123
	v_exp_f32_e32 v76, v124
	v_exp_f32_e32 v77, v125
	ds_read_b128 v[202:205], v3 offset:2048
	ds_read_b128 v[186:189], v3 offset:2560
	v_mfma_f32_32x32x16_bf16 v[34:49], v[182:185], v[214:217], v[34:49]
	v_exp_f32_e32 v78, v126
	v_exp_f32_e32 v79, v127
	v_exp_f32_e32 v80, v128
	v_exp_f32_e32 v81, v129
	ds_read_b128 v[198:201], v3 offset:4096
	ds_read_b128 v[182:185], v3 offset:4608
	v_mfma_f32_32x32x16_bf16 v[18:33], v[178:181], v[210:213], v[18:33]
	v_exp_f32_e32 v50, v98
	v_exp_f32_e32 v51, v99
	v_exp_f32_e32 v52, v100
	v_exp_f32_e32 v53, v101
	ds_read_b128 v[190:193], v3 offset:6144
	ds_read_b128 v[170:173], v3 offset:6656
	v_mfma_f32_32x32x16_bf16 v[34:49], v[178:181], v[12:15], v[34:49]
	v_exp_f32_e32 v54, v102
	v_exp_f32_e32 v55, v103
	v_exp_f32_e32 v56, v104
	v_exp_f32_e32 v57, v105
	ds_read_b128 v[178:181], v3 offset:8192
	ds_read_b128 v[166:169], v3 offset:8704
	v_mfma_f32_32x32x16_bf16 v[18:33], v[218:221], v[8:11], v[18:33]
	v_exp_f32_e32 v58, v106
	v_exp_f32_e32 v59, v107
	v_exp_f32_e32 v60, v108
	v_exp_f32_e32 v61, v109
	ds_read_b128 v[174:177], v3 offset:10240
	ds_read_b128 v[162:165], v3 offset:10752
	v_mfma_f32_32x32x16_bf16 v[34:49], v[218:221], v[4:7], v[34:49]
	v_exp_f32_e32 v62, v110
	v_exp_f32_e32 v63, v111
	v_exp_f32_e32 v64, v112
	v_exp_f32_e32 v65, v113
	s_mov_b32 s26, s27
	s_cmp_eq_u32 s27, s96
	s_cbranch_scc1 .Lmla_ss1_xdone
	s_add_i32 s64, s27, 3
	s_cmp_lt_u32 s64, s94
	s_cbranch_scc1 .Lmla_ss1_top
	s_waitcnt vmcnt(4)
	s_barrier
	s_branch .Lmla_ss_back

; #define SFENCE() __builtin_amdgcn_sched_barrier(0)
; template <bool FOX>
; __device__ __forceinline__ void attn_unit(const Args& A, int b, int h, int qb, LAS char* shm, LAS float* dg) {
;     ...
;           const lds_cptr vp = vp0 + ((t - 1) % NS) * VSLOT; float sa = 0.f, sb = 0.f;
; #pragma unroll
;           for (int g = 0; g < 2 * NQ; ++g) {
;               if (!FOX && g == 0) c0 = __builtin_amdgcn_mfma_f32_32x32x16_bf16(kf[0], qr[0], negm, 0, 0, 0);
;               else if (!FOX && g == 1) c1 = __builtin_amdgcn_mfma_f32_32x32x16_bf16(kf[1], qr[0], negm, 0, 0, 0);
;               else if (g & 1) c1 = __builtin_amdgcn_mfma_f32_32x32x16_bf16(kf[g], qr[g >> 1], c1, 0, 0, 0); else c0 = __builtin_amdgcn_mfma_f32_32x32x16_bf16(kf[g], qr[g >> 1], c0, 0, 0, 0);
;               if (g < 8) { const int i = (g >> 1) + 4 * (g & 1); vlo[i] = vtr(vp + (i >> 2) * 4096 + (i & 3) * 1024); vhi[i] = vtr(vp + (i >> 2) * 4096 + (i & 3) * 1024 + 512);
;                   if (g < 4) { sa += pp0[4 * g]; sb += pp0[4 * g + 1]; sa += pp0[4 * g + 2]; sb += pp0[4 * g + 3]; } else { sa += pp1[4 * g - 16]; sb += pp1[4 * g - 15]; sa += pp1[4 * g - 14]; sb += pp1[4 * g - 13]; }
;                   asm volatile("" : "+v"(sa), "+v"(sb)); }
;               { constexpr int G0 = FOX ? 0 : 4; if (g >= G0) { const int q = 2 * (g - G0);
; #pragma unroll
;                   for (int k = 0; k < 2; ++k) { const int w = q + k; const unsigned pkd = w < 8 ? cvt_pk_bf16(pp0[2 * w], pp0[2 * w + 1]) : cvt_pk_bf16(pp1[2 * w - 16], pp1[2 * w - 15]); pw[w >> 2][w & 3] = pkd; } } }
;               SFENCE();
;           }
;           lrun += sa + sb; }
;         MASKONLY(t);
;         float rm; ROWMAX(rm);
;         bool resc = false;
;         if (__any(rm > THR)) { const float dl = fmaxf(rm, 0.f); mhat += dl;
; #pragma unroll
;             for (int r = 0; r < 16; ++r) { c0[r] -= dl; c1[r] -= dl; }
;             if constexpr (!FOX) {
; #pragma unroll
;                 for (int r = 0; r < 16; ++r) negm[r] = -mhat;
;                 asm volatile("" : "+v"(negm)); }
;             const float f = __builtin_amdgcn_exp2f(-dl); lrun *= f; if (hi == 0) wsf[r32] = f; resc = true; }
;         SFENCE();
;         { const lds_cptr kp = kp0 + ((t + 1) % NS) * KSLOT;
; #pragma unroll
;           for (int g = 0; g < 8; ++g) { const int i = (g >> 1) + 4 * (g & 1);
.Lmla_ss2_top:
	s_mov_b32 m0, s52
	s_nop 0
	global_load_lds_dwordx4 v240, s[46:47]
	s_mov_b32 m0, s53
	s_nop 0
	global_load_lds_dwordx4 v240, s[60:61]
	s_waitcnt lgkmcnt(0)
	s_add_i32 s27, s42, 0x8000
	v_mfma_f32_32x32x16_bf16 v[114:129], v[206:209], v[138:141], v[82:97]
	s_and_b32 s27, s27, 0x6000
	s_add_u32 s42, s42, 0x2000
	s_addc_u32 s43, s43, 0
	v_add_u32_e32 v3, s27, v247
	ds_read_b64_tr_b16 v[206:207], v3 offset:49152
	ds_read_b64_tr_b16 v[208:209], v3 offset:49664
	v_add_f32_e32 v4, 0, v67
	v_add_f32_e32 v5, 0, v66
	v_add_f32_e32 v4, v69, v4
	v_add_f32_e32 v5, v68, v5
	v_mfma_f32_32x32x16_bf16 v[98:113], v[194:197], v[138:141], v[82:97]
	ds_read_b64_tr_b16 v[194:195], v3 offset:53248
	ds_read_b64_tr_b16 v[196:197], v3 offset:53760
	v_add_f32_e32 v4, v71, v4
	v_add_f32_e32 v5, v70, v5
	v_add_f32_e32 v4, v73, v4
	v_add_f32_e32 v5, v72, v5
	v_mfma_f32_32x32x16_bf16 v[114:129], v[202:205], v[142:145], v[114:129]
	ds_read_b64_tr_b16 v[202:203], v3 offset:50176
	ds_read_b64_tr_b16 v[204:205], v3 offset:50688
	v_add_f32_e32 v4, v75, v4
	v_add_f32_e32 v5, v74, v5
	v_add_f32_e32 v4, v77, v4
	v_add_f32_e32 v5, v76, v5
	v_mfma_f32_32x32x16_bf16 v[98:113], v[186:189], v[142:145], v[98:113]
	ds_read_b64_tr_b16 v[214:215], v3 offset:54272
	ds_read_b64_tr_b16 v[216:217], v3 offset:54784
	v_add_f32_e32 v4, v79, v4
	v_add_f32_e32 v5, v78, v5
	v_add_f32_e32 v4, v81, v4
	v_add_f32_e32 v5, v80, v5
	v_mfma_f32_32x32x16_bf16 v[114:129], v[198:201], v[146:149], v[114:129]
	ds_read_b64_tr_b16 v[210:211], v3 offset:51200
	ds_read_b64_tr_b16 v[212:213], v3 offset:51712
	v_add_f32_e32 v4, v51, v4
	v_add_f32_e32 v5, v50, v5
	v_add_f32_e32 v4, v53, v4
	v_add_f32_e32 v5, v52, v5
	v_mfma_f32_32x32x16_bf16 v[98:113], v[182:185], v[146:149], v[98:113]
	ds_read_b64_tr_b16 v[12:13], v3 offset:55296
	ds_read_b64_tr_b16 v[14:15], v3 offset:55808
	v_add_f32_e32 v4, v55, v4
	v_add_f32_e32 v5, v54, v5
	v_add_f32_e32 v4, v57, v4
	v_add_f32_e32 v5, v56, v5
	v_mfma_f32_32x32x16_bf16 v[114:129], v[190:193], v[150:153], v[114:129]
	ds_read_b64_tr_b16 v[8:9], v3 offset:52224
	ds_read_b64_tr_b16 v[10:11], v3 offset:52736
	v_add_f32_e32 v4, v59, v4
	v_add_f32_e32 v16, v61, v4
	v_add_f32_e32 v4, v58, v5
	v_add_f32_e32 v17, v60, v4
	v_mfma_f32_32x32x16_bf16 v[98:113], v[170:173], v[150:153], v[98:113]
	s_add_u32 s46, s46, s62
	s_addc_u32 s47, s47, s63
	s_and_b32 s64, s26, 3
	ds_read_b64_tr_b16 v[4:5], v3 offset:56320
	ds_read_b64_tr_b16 v[6:7], v3 offset:56832
	v_add_f32_e32 v3, v63, v16
	v_add_f32_e32 v16, v62, v17
	v_add_f32_e32 v3, v65, v3
	v_add_f32_e32 v16, v64, v16
	v_mfma_f32_32x32x16_bf16 v[114:129], v[178:181], v[154:157], v[114:129]
	s_mulk_i32 s64, 0x3000
	s_add_u32 s60, s60, 0x2000
	s_addc_u32 s61, s61, 0
	v_cvt_pk_bf16_f32 v178, v50, v51
	v_cvt_pk_bf16_f32 v179, v52, v53
	v_cvt_pk_bf16_f32 v186, v66, v67
	v_cvt_pk_bf16_f32 v187, v68, v69
	v_mfma_f32_32x32x16_bf16 v[98:113], v[166:169], v[154:157], v[98:113]
	s_add_i32 s52, s64, s91
	s_add_i32 s64, s42, 0x6000
	v_cvt_pk_bf16_f32 v180, v54, v55
	v_cvt_pk_bf16_f32 v181, v56, v57
	v_cvt_pk_bf16_f32 v188, v70, v71
	v_cvt_pk_bf16_f32 v189, v72, v73
	v_mfma_f32_32x32x16_bf16 v[114:129], v[174:177], v[158:161], v[114:129]
	s_and_b32 s64, s64, 0x6000
	s_add_i32 s53, s64, s93
	v_cvt_pk_bf16_f32 v218, v58, v59
	v_cvt_pk_bf16_f32 v219, v60, v61
	v_cvt_pk_bf16_f32 v182, v74, v75
	v_cvt_pk_bf16_f32 v183, v76, v77
	v_mfma_f32_32x32x16_bf16 v[98:113], v[162:165], v[158:161], v[98:113]
	v_cvt_pk_bf16_f32 v220, v62, v63
	v_cvt_pk_bf16_f32 v221, v64, v65
	v_cvt_pk_bf16_f32 v184, v78, v79
	v_cvt_pk_bf16_f32 v185, v80, v81
	v_add_f32_e32 v3, v3, v16
	v_add_f32_e32 v246, v246, v3
	s_waitcnt vmcnt(3)
	s_waitcnt lgkmcnt(0)
	s_barrier
	v_mfma_f32_32x32x16_bf16 v[18:33], v[186:189], v[206:209], v[18:33]
	s_add_i32 s27, s26, 1
	s_and_b32 s64, s27, 3
	s_mulk_i32 s64, 0x3000
	v_exp_f32_e32 v66, v114
	v_exp_f32_e32 v67, v115
	v_exp_f32_e32 v68, v116
	v_exp_f32_e32 v69, v117
	v_add_u32_e32 v3, s64, v248
	v_mfma_f32_32x32x16_bf16 v[34:49], v[186:189], v[194:197], v[34:49]
	v_exp_f32_e32 v70, v118
	v_exp_f32_e32 v71, v119
	v_exp_f32_e32 v72, v120
	v_exp_f32_e32 v73, v121
	ds_read_b128 v[206:209], v3
	ds_read_b128 v[194:197], v3 offset:512
	v_mfma_f32_32x32x16_bf16 v[18:33], v[182:185], v[202:205], v[18:33]
	v_exp_f32_e32 v74, v122
	v_exp_f32_e32 v75, v123
	v_exp_f32_e32 v76, v124
	v_exp_f32_e32 v77, v125
	ds_read_b128 v[202:205], v3 offset:2048
	ds_read_b128 v[186:189], v3 offset:2560
	v_mfma_f32_32x32x16_bf16 v[34:49], v[182:185], v[214:217], v[34:49]
	v_exp_f32_e32 v78, v126
	v_exp_f32_e32 v79, v127
	v_exp_f32_e32 v80, v128
	v_exp_f32_e32 v81, v129
	ds_read_b128 v[198:201], v3 offset:4096
	ds_read_b128 v[182:185], v3 offset:4608
	v_mfma_f32_32x32x16_bf16 v[18:33], v[178:181], v[210:213], v[18:33]
	v_exp_f32_e32 v50, v98
	v_exp_f32_e32 v51, v99
	v_exp_f32_e32 v52, v100
	v_exp_f32_e32 v53, v101
	ds_read_b128 v[190:193], v3 offset:6144
	ds_read_b128 v[170:173], v3 offset:6656
	v_mfma_f32_32x32x16_bf16 v[34:49], v[178:181], v[12:15], v[34:49]
	v_exp_f32_e32 v54, v102
	v_exp_f32_e32 v55, v103
	v_exp_f32_e32 v56, v104
	v_exp_f32_e32 v57, v105
	ds_read_b128 v[178:181], v3 offset:8192
	ds_read_b128 v[166:169], v3 offset:8704
	v_mfma_f32_32x32x16_bf16 v[18:33], v[218:221], v[8:11], v[18:33]
	v_exp_f32_e32 v58, v106
	v_exp_f32_e32 v59, v107
	v_exp_f32_e32 v60, v108
	v_exp_f32_e32 v61, v109
	ds_read_b128 v[174:177], v3 offset:10240
	ds_read_b128 v[162:165], v3 offset:10752
	v_mfma_f32_32x32x16_bf16 v[34:49], v[218:221], v[4:7], v[34:49]
	v_exp_f32_e32 v62, v110
	v_exp_f32_e32 v63, v111
	v_exp_f32_e32 v64, v112
	v_exp_f32_e32 v65, v113
	s_mov_b32 s26, s27
	s_cmp_eq_u32 s27, s96
	s_cbranch_scc1 .Lmla_ss2_xdone
	s_add_i32 s64, s27, 3
	s_cmp_lt_u32 s64, s94
	s_cbranch_scc1 .Lmla_ss2_top
	s_branch .Lmla_ss_back

; template <bool FOX>
; __device__ __forceinline__ void attn_unit(const Args& A, int b, int h, int qb, LAS char* shm, LAS float* dg) {
;     ...
;     const bf16_t* Kg = (FOX ? A.Fk : A.Kmla) + (long)(b * 8 + h) * 128 * (KSLOT / 2) + wid * 512 + lane * 8;
;     const bf16_t* Vg = (FOX ? A.Fv : A.Vmla) + (long)(b * 8 + h) * 128 * 4096 + wid * 512 + lane * 8;
;     const unsigned kdst = lds0 + L_K + wid * 1024, vdst = lds0 + L_V + wid * 1024;
;     const bool k2 = (!FOX) && wid < 4;
.Lmla_ss_back:
	v_mov_b32_e32 v235, s47
	v_add_co_u32_e32 v234, vcc, s46, v240
	s_nop 1
	v_addc_co_u32_e32 v235, vcc, 0, v235, vcc
	s_mov_b32 s98, 1
	s_waitcnt lgkmcnt(0)
	s_mov_b64 s[60:61], 0
	s_branch .LBB0_825
.Lmla_ss_done:
	v_mov_b32_e32 v235, s47
	v_add_co_u32_e32 v234, vcc, s46, v240
	s_nop 1
	v_addc_co_u32_e32 v235, vcc, 0, v235, vcc
	s_mov_b32 s98, 1
	s_waitcnt lgkmcnt(0)
	s_mov_b64 s[46:47], -1
	s_mov_b64 s[52:53], -1
	s_mov_b64 s[60:61], 0
	s_branch .LBB0_867
